# gate epilogue with packed f32 fma/add + saturating pack; out-proj redundant zeroing removed
# baseline (speedup 1.0000x reference)
.LBB0_853:
	s_waitcnt lgkmcnt(0)
	s_mov_b32 s98, 0xbfb8aa3b
	s_mov_b32 s99, 0xbfb8aa3b
	v_pk_fma_f32 v[160:161], v[160:161], s[98:99], v[184:185]
	v_pk_fma_f32 v[162:163], v[162:163], s[98:99], v[186:187]
	v_pk_fma_f32 v[156:157], v[156:157], s[98:99], v[180:181]
	v_pk_fma_f32 v[158:159], v[158:159], s[98:99], v[182:183]
	v_pk_fma_f32 v[152:153], v[152:153], s[98:99], v[188:189]
	v_pk_fma_f32 v[154:155], v[154:155], s[98:99], v[190:191]
	v_pk_fma_f32 v[148:149], v[148:149], s[98:99], v[192:193]
	v_pk_fma_f32 v[150:151], v[150:151], s[98:99], v[194:195]
	v_mov_b32_e32 v188, 1.0
	v_mov_b32_e32 v189, 1.0
	v_mov_b32_e32 v223, 0
	s_add_i32 s19, s87, -11
	s_lshr_b32 s20, s19, 2
	v_mov_b32_e32 v184, s20
	v_mov_b32_e32 v185, v3
	v_mad_i64_i32 v[184:185], s[20:21], v220, 3, v[184:185]
	v_lshlrev_b64 v[184:185], 10, v[184:185]
	s_lshl_b32 s19, s19, 8
	s_and_b32 s34, s19, 0x300
	v_lshl_add_u64 v[184:185], s[46:47], 0, v[184:185]
	v_lshl_add_u64 v[184:185], v[184:185], 0, s[34:35]
	v_lshl_add_u64 v[186:187], v[184:185], 0, v[2:3]
	v_exp_f32_e32 v160, v160
	v_exp_f32_e32 v161, v161
	v_exp_f32_e32 v162, v162
	v_exp_f32_e32 v163, v163
	v_exp_f32_e32 v156, v156
	v_exp_f32_e32 v157, v157
	v_exp_f32_e32 v158, v158
	v_exp_f32_e32 v159, v159
	v_exp_f32_e32 v152, v152
	v_exp_f32_e32 v153, v153
	v_exp_f32_e32 v154, v154
	v_exp_f32_e32 v155, v155
	v_exp_f32_e32 v148, v148
	v_exp_f32_e32 v149, v149
	v_exp_f32_e32 v150, v150
	v_exp_f32_e32 v151, v151
	v_pk_add_f32 v[160:161], v[160:161], v[188:189]
	v_pk_add_f32 v[162:163], v[162:163], v[188:189]
	v_pk_add_f32 v[156:157], v[156:157], v[188:189]
	v_pk_add_f32 v[158:159], v[158:159], v[188:189]
	v_pk_add_f32 v[152:153], v[152:153], v[188:189]
	v_pk_add_f32 v[154:155], v[154:155], v[188:189]
	v_pk_add_f32 v[148:149], v[148:149], v[188:189]
	v_pk_add_f32 v[150:151], v[150:151], v[188:189]
	v_rcp_f32_e32 v160, v160
	v_rcp_f32_e32 v161, v161
	v_rcp_f32_e32 v162, v162
	v_rcp_f32_e32 v163, v163
	v_rcp_f32_e32 v156, v156
	v_rcp_f32_e32 v157, v157
	v_rcp_f32_e32 v158, v158
	v_rcp_f32_e32 v159, v159
	v_rcp_f32_e32 v152, v152
	v_rcp_f32_e32 v153, v153
	v_rcp_f32_e32 v154, v154
	v_rcp_f32_e32 v155, v155
	v_rcp_f32_e32 v148, v148
	v_rcp_f32_e32 v149, v149
	v_rcp_f32_e32 v150, v150
	v_rcp_f32_e32 v151, v151
	v_add_u32_e32 v160, 0xc4820000, v160
	v_add_u32_e32 v161, 0xc4820000, v161
	v_add_u32_e32 v162, 0xc4820000, v162
	v_add_u32_e32 v163, 0xc4820000, v163
	v_add_u32_e32 v156, 0xc4820000, v156
	v_add_u32_e32 v157, 0xc4820000, v157
	v_add_u32_e32 v158, 0xc4820000, v158
	v_add_u32_e32 v159, 0xc4820000, v159
	v_add_u32_e32 v152, 0xc4820000, v152
	v_add_u32_e32 v153, 0xc4820000, v153
	v_add_u32_e32 v154, 0xc4820000, v154
	v_add_u32_e32 v155, 0xc4820000, v155
	v_add_u32_e32 v148, 0xc4820000, v148
	v_add_u32_e32 v149, 0xc4820000, v149
	v_add_u32_e32 v150, 0xc4820000, v150
	v_add_u32_e32 v151, 0xc4820000, v151
	v_ashr_pk_u8_i32 v160, v160, v161, 18
	v_ashr_pk_u8_i32 v162, v162, v163, 18
	v_ashr_pk_u8_i32 v156, v156, v157, 18
	v_ashr_pk_u8_i32 v158, v158, v159, 18
	v_ashr_pk_u8_i32 v152, v152, v153, 18
	v_ashr_pk_u8_i32 v154, v154, v155, 18
	v_ashr_pk_u8_i32 v148, v148, v149, 18
	v_ashr_pk_u8_i32 v150, v150, v151, 18
	v_and_b32_e32 v160, 0xffff, v160
	v_lshl_or_b32 v180, v162, 16, v160
	v_and_b32_e32 v156, 0xffff, v156
	v_lshl_or_b32 v181, v158, 16, v156
	v_and_b32_e32 v152, 0xffff, v152
	v_lshl_or_b32 v182, v154, 16, v152
	v_and_b32_e32 v148, 0xffff, v148
	v_lshl_or_b32 v183, v150, 16, v148
	global_store_dwordx4 v[186:187], v[180:183], off
	s_and_b64 vcc, exec, s[40:41]
	s_mov_b64 s[26:27], -1
	s_cbranch_vccz .LBB0_925

.LBB0_855:
	s_waitcnt lgkmcnt(0)
	s_mov_b32 s98, 0xbfb8aa3b
	s_mov_b32 s99, 0xbfb8aa3b
	v_pk_fma_f32 v[128:129], v[128:129], s[98:99], v[168:169]
	v_pk_fma_f32 v[130:131], v[130:131], s[98:99], v[170:171]
	v_pk_fma_f32 v[124:125], v[124:125], s[98:99], v[164:165]
	v_pk_fma_f32 v[126:127], v[126:127], s[98:99], v[166:167]
	v_pk_fma_f32 v[120:121], v[120:121], s[98:99], v[172:173]
	v_pk_fma_f32 v[122:123], v[122:123], s[98:99], v[174:175]
	v_pk_fma_f32 v[116:117], v[116:117], s[98:99], v[176:177]
	v_pk_fma_f32 v[118:119], v[118:119], s[98:99], v[178:179]
	v_mov_b32_e32 v172, 1.0
	v_mov_b32_e32 v173, 1.0
	v_mov_b32_e32 v150, v223
	s_add_i32 s19, s87, -11
	s_lshr_b32 s20, s19, 2
	v_mov_b32_e32 v168, s20
	v_mov_b32_e32 v169, v3
	v_mad_i64_i32 v[168:169], s[20:21], v226, 3, v[168:169]
	v_lshlrev_b64 v[168:169], 10, v[168:169]
	s_lshl_b32 s19, s19, 8
	s_and_b32 s34, s19, 0x300
	v_lshl_add_u64 v[168:169], s[46:47], 0, v[168:169]
	v_lshl_add_u64 v[168:169], v[168:169], 0, s[34:35]
	v_lshl_add_u64 v[170:171], v[168:169], 0, v[2:3]
	v_exp_f32_e32 v128, v128
	v_exp_f32_e32 v129, v129
	v_exp_f32_e32 v130, v130
	v_exp_f32_e32 v131, v131
	v_exp_f32_e32 v124, v124
	v_exp_f32_e32 v125, v125
	v_exp_f32_e32 v126, v126
	v_exp_f32_e32 v127, v127
	v_exp_f32_e32 v120, v120
	v_exp_f32_e32 v121, v121
	v_exp_f32_e32 v122, v122
	v_exp_f32_e32 v123, v123
	v_exp_f32_e32 v116, v116
	v_exp_f32_e32 v117, v117
	v_exp_f32_e32 v118, v118
	v_exp_f32_e32 v119, v119
	v_pk_add_f32 v[128:129], v[128:129], v[172:173]
	v_pk_add_f32 v[130:131], v[130:131], v[172:173]
	v_pk_add_f32 v[124:125], v[124:125], v[172:173]
	v_pk_add_f32 v[126:127], v[126:127], v[172:173]
	v_pk_add_f32 v[120:121], v[120:121], v[172:173]
	v_pk_add_f32 v[122:123], v[122:123], v[172:173]
	v_pk_add_f32 v[116:117], v[116:117], v[172:173]
	v_pk_add_f32 v[118:119], v[118:119], v[172:173]
	v_rcp_f32_e32 v128, v128
	v_rcp_f32_e32 v129, v129
	v_rcp_f32_e32 v130, v130
	v_rcp_f32_e32 v131, v131
	v_rcp_f32_e32 v124, v124
	v_rcp_f32_e32 v125, v125
	v_rcp_f32_e32 v126, v126
	v_rcp_f32_e32 v127, v127
	v_rcp_f32_e32 v120, v120
	v_rcp_f32_e32 v121, v121
	v_rcp_f32_e32 v122, v122
	v_rcp_f32_e32 v123, v123
	v_rcp_f32_e32 v116, v116
	v_rcp_f32_e32 v117, v117
	v_rcp_f32_e32 v118, v118
	v_rcp_f32_e32 v119, v119
	v_add_u32_e32 v128, 0xc4820000, v128
	v_add_u32_e32 v129, 0xc4820000, v129
	v_add_u32_e32 v130, 0xc4820000, v130
	v_add_u32_e32 v131, 0xc4820000, v131
	v_add_u32_e32 v124, 0xc4820000, v124
	v_add_u32_e32 v125, 0xc4820000, v125
	v_add_u32_e32 v126, 0xc4820000, v126
	v_add_u32_e32 v127, 0xc4820000, v127
	v_add_u32_e32 v120, 0xc4820000, v120
	v_add_u32_e32 v121, 0xc4820000, v121
	v_add_u32_e32 v122, 0xc4820000, v122
	v_add_u32_e32 v123, 0xc4820000, v123
	v_add_u32_e32 v116, 0xc4820000, v116
	v_add_u32_e32 v117, 0xc4820000, v117
	v_add_u32_e32 v118, 0xc4820000, v118
	v_add_u32_e32 v119, 0xc4820000, v119
	v_ashr_pk_u8_i32 v128, v128, v129, 18
	v_ashr_pk_u8_i32 v130, v130, v131, 18
	v_ashr_pk_u8_i32 v124, v124, v125, 18
	v_ashr_pk_u8_i32 v126, v126, v127, 18
	v_ashr_pk_u8_i32 v120, v120, v121, 18
	v_ashr_pk_u8_i32 v122, v122, v123, 18
	v_ashr_pk_u8_i32 v116, v116, v117, 18
	v_ashr_pk_u8_i32 v118, v118, v119, 18
	v_and_b32_e32 v128, 0xffff, v128
	v_lshl_or_b32 v164, v130, 16, v128
	v_and_b32_e32 v124, 0xffff, v124
	v_lshl_or_b32 v165, v126, 16, v124
	v_and_b32_e32 v120, 0xffff, v120
	v_lshl_or_b32 v166, v122, 16, v120
	v_and_b32_e32 v116, 0xffff, v116
	v_lshl_or_b32 v167, v118, 16, v116
	global_store_dwordx4 v[170:171], v[164:167], off
	s_and_b64 vcc, exec, s[40:41]
	s_mov_b64 s[26:27], -1
	s_cbranch_vccz .LBB0_975

.LBB0_857:
	s_waitcnt lgkmcnt(0)
	s_mov_b32 s98, 0xbfb8aa3b
	s_mov_b32 s99, 0xbfb8aa3b
	v_pk_fma_f32 v[96:97], v[96:97], s[98:99], v[136:137]
	v_pk_fma_f32 v[98:99], v[98:99], s[98:99], v[138:139]
	v_pk_fma_f32 v[92:93], v[92:93], s[98:99], v[132:133]
	v_pk_fma_f32 v[94:95], v[94:95], s[98:99], v[134:135]
	v_pk_fma_f32 v[88:89], v[88:89], s[98:99], v[140:141]
	v_pk_fma_f32 v[90:91], v[90:91], s[98:99], v[142:143]
	v_pk_fma_f32 v[84:85], v[84:85], s[98:99], v[144:145]
	v_pk_fma_f32 v[86:87], v[86:87], s[98:99], v[146:147]
	v_mov_b32_e32 v140, 1.0
	v_mov_b32_e32 v141, 1.0
	v_mov_b32_e32 v118, v150
	s_add_i32 s19, s87, -11
	s_lshr_b32 s20, s19, 2
	v_mov_b32_e32 v136, s20
	v_mov_b32_e32 v137, v3
	v_mad_i64_i32 v[136:137], s[20:21], v224, 3, v[136:137]
	v_lshlrev_b64 v[136:137], 10, v[136:137]
	s_lshl_b32 s19, s19, 8
	s_and_b32 s34, s19, 0x300
	v_lshl_add_u64 v[136:137], s[46:47], 0, v[136:137]
	v_lshl_add_u64 v[136:137], v[136:137], 0, s[34:35]
	v_lshl_add_u64 v[138:139], v[136:137], 0, v[2:3]
	v_exp_f32_e32 v96, v96
	v_exp_f32_e32 v97, v97
	v_exp_f32_e32 v98, v98
	v_exp_f32_e32 v99, v99
	v_exp_f32_e32 v92, v92
	v_exp_f32_e32 v93, v93
	v_exp_f32_e32 v94, v94
	v_exp_f32_e32 v95, v95
	v_exp_f32_e32 v88, v88
	v_exp_f32_e32 v89, v89
	v_exp_f32_e32 v90, v90
	v_exp_f32_e32 v91, v91
	v_exp_f32_e32 v84, v84
	v_exp_f32_e32 v85, v85
	v_exp_f32_e32 v86, v86
	v_exp_f32_e32 v87, v87
	v_pk_add_f32 v[96:97], v[96:97], v[140:141]
	v_pk_add_f32 v[98:99], v[98:99], v[140:141]
	v_pk_add_f32 v[92:93], v[92:93], v[140:141]
	v_pk_add_f32 v[94:95], v[94:95], v[140:141]
	v_pk_add_f32 v[88:89], v[88:89], v[140:141]
	v_pk_add_f32 v[90:91], v[90:91], v[140:141]
	v_pk_add_f32 v[84:85], v[84:85], v[140:141]
	v_pk_add_f32 v[86:87], v[86:87], v[140:141]
	v_rcp_f32_e32 v96, v96
	v_rcp_f32_e32 v97, v97
	v_rcp_f32_e32 v98, v98
	v_rcp_f32_e32 v99, v99
	v_rcp_f32_e32 v92, v92
	v_rcp_f32_e32 v93, v93
	v_rcp_f32_e32 v94, v94
	v_rcp_f32_e32 v95, v95
	v_rcp_f32_e32 v88, v88
	v_rcp_f32_e32 v89, v89
	v_rcp_f32_e32 v90, v90
	v_rcp_f32_e32 v91, v91
	v_rcp_f32_e32 v84, v84
	v_rcp_f32_e32 v85, v85
	v_rcp_f32_e32 v86, v86
	v_rcp_f32_e32 v87, v87
	v_add_u32_e32 v96, 0xc4820000, v96
	v_add_u32_e32 v97, 0xc4820000, v97
	v_add_u32_e32 v98, 0xc4820000, v98
	v_add_u32_e32 v99, 0xc4820000, v99
	v_add_u32_e32 v92, 0xc4820000, v92
	v_add_u32_e32 v93, 0xc4820000, v93
	v_add_u32_e32 v94, 0xc4820000, v94
	v_add_u32_e32 v95, 0xc4820000, v95
	v_add_u32_e32 v88, 0xc4820000, v88
	v_add_u32_e32 v89, 0xc4820000, v89
	v_add_u32_e32 v90, 0xc4820000, v90
	v_add_u32_e32 v91, 0xc4820000, v91
	v_add_u32_e32 v84, 0xc4820000, v84
	v_add_u32_e32 v85, 0xc4820000, v85
	v_add_u32_e32 v86, 0xc4820000, v86
	v_add_u32_e32 v87, 0xc4820000, v87
	v_ashr_pk_u8_i32 v96, v96, v97, 18
	v_ashr_pk_u8_i32 v98, v98, v99, 18
	v_ashr_pk_u8_i32 v92, v92, v93, 18
	v_ashr_pk_u8_i32 v94, v94, v95, 18
	v_ashr_pk_u8_i32 v88, v88, v89, 18
	v_ashr_pk_u8_i32 v90, v90, v91, 18
	v_ashr_pk_u8_i32 v84, v84, v85, 18
	v_ashr_pk_u8_i32 v86, v86, v87, 18
	v_and_b32_e32 v96, 0xffff, v96
	v_lshl_or_b32 v132, v98, 16, v96
	v_and_b32_e32 v92, 0xffff, v92
	v_lshl_or_b32 v133, v94, 16, v92
	v_and_b32_e32 v88, 0xffff, v88
	v_lshl_or_b32 v134, v90, 16, v88
	v_and_b32_e32 v84, 0xffff, v84
	v_lshl_or_b32 v135, v86, 16, v84
	global_store_dwordx4 v[138:139], v[132:135], off
	s_and_b64 vcc, exec, s[40:41]
	s_mov_b64 s[26:27], -1
	s_cbranch_vccz .LBB0_1025

.LBB0_859:
	s_waitcnt lgkmcnt(0)
	s_mov_b32 s98, 0xbfb8aa3b
	s_mov_b32 s99, 0xbfb8aa3b
	v_pk_fma_f32 v[80:81], v[80:81], s[98:99], v[104:105]
	v_pk_fma_f32 v[82:83], v[82:83], s[98:99], v[106:107]
	v_pk_fma_f32 v[76:77], v[76:77], s[98:99], v[100:101]
	v_pk_fma_f32 v[78:79], v[78:79], s[98:99], v[102:103]
	v_pk_fma_f32 v[72:73], v[72:73], s[98:99], v[108:109]
	v_pk_fma_f32 v[74:75], v[74:75], s[98:99], v[110:111]
	v_pk_fma_f32 v[68:69], v[68:69], s[98:99], v[112:113]
	v_pk_fma_f32 v[70:71], v[70:71], s[98:99], v[114:115]
	v_mov_b32_e32 v108, 1.0
	v_mov_b32_e32 v109, 1.0
	v_mov_b32_e32 v142, v118
	s_add_i32 s19, s87, -11
	s_lshr_b32 s20, s19, 2
	v_mov_b32_e32 v104, s20
	v_mov_b32_e32 v105, v3
	v_mad_i64_i32 v[104:105], s[20:21], v222, 3, v[104:105]
	v_lshlrev_b64 v[104:105], 10, v[104:105]
	s_lshl_b32 s19, s19, 8
	s_and_b32 s34, s19, 0x300
	v_lshl_add_u64 v[104:105], s[46:47], 0, v[104:105]
	v_lshl_add_u64 v[104:105], v[104:105], 0, s[34:35]
	v_lshl_add_u64 v[106:107], v[104:105], 0, v[2:3]
	v_exp_f32_e32 v80, v80
	v_exp_f32_e32 v81, v81
	v_exp_f32_e32 v82, v82
	v_exp_f32_e32 v83, v83
	v_exp_f32_e32 v76, v76
	v_exp_f32_e32 v77, v77
	v_exp_f32_e32 v78, v78
	v_exp_f32_e32 v79, v79
	v_exp_f32_e32 v72, v72
	v_exp_f32_e32 v73, v73
	v_exp_f32_e32 v74, v74
	v_exp_f32_e32 v75, v75
	v_exp_f32_e32 v68, v68
	v_exp_f32_e32 v69, v69
	v_exp_f32_e32 v70, v70
	v_exp_f32_e32 v71, v71
	v_pk_add_f32 v[80:81], v[80:81], v[108:109]
	v_pk_add_f32 v[82:83], v[82:83], v[108:109]
	v_pk_add_f32 v[76:77], v[76:77], v[108:109]
	v_pk_add_f32 v[78:79], v[78:79], v[108:109]
	v_pk_add_f32 v[72:73], v[72:73], v[108:109]
	v_pk_add_f32 v[74:75], v[74:75], v[108:109]
	v_pk_add_f32 v[68:69], v[68:69], v[108:109]
	v_pk_add_f32 v[70:71], v[70:71], v[108:109]
	v_rcp_f32_e32 v80, v80
	v_rcp_f32_e32 v81, v81
	v_rcp_f32_e32 v82, v82
	v_rcp_f32_e32 v83, v83
	v_rcp_f32_e32 v76, v76
	v_rcp_f32_e32 v77, v77
	v_rcp_f32_e32 v78, v78
	v_rcp_f32_e32 v79, v79
	v_rcp_f32_e32 v72, v72
	v_rcp_f32_e32 v73, v73
	v_rcp_f32_e32 v74, v74
	v_rcp_f32_e32 v75, v75
	v_rcp_f32_e32 v68, v68
	v_rcp_f32_e32 v69, v69
	v_rcp_f32_e32 v70, v70
	v_rcp_f32_e32 v71, v71
	v_add_u32_e32 v80, 0xc4820000, v80
	v_add_u32_e32 v81, 0xc4820000, v81
	v_add_u32_e32 v82, 0xc4820000, v82
	v_add_u32_e32 v83, 0xc4820000, v83
	v_add_u32_e32 v76, 0xc4820000, v76
	v_add_u32_e32 v77, 0xc4820000, v77
	v_add_u32_e32 v78, 0xc4820000, v78
	v_add_u32_e32 v79, 0xc4820000, v79
	v_add_u32_e32 v72, 0xc4820000, v72
	v_add_u32_e32 v73, 0xc4820000, v73
	v_add_u32_e32 v74, 0xc4820000, v74
	v_add_u32_e32 v75, 0xc4820000, v75
	v_add_u32_e32 v68, 0xc4820000, v68
	v_add_u32_e32 v69, 0xc4820000, v69
	v_add_u32_e32 v70, 0xc4820000, v70
	v_add_u32_e32 v71, 0xc4820000, v71
	v_ashr_pk_u8_i32 v80, v80, v81, 18
	v_ashr_pk_u8_i32 v82, v82, v83, 18
	v_ashr_pk_u8_i32 v76, v76, v77, 18
	v_ashr_pk_u8_i32 v78, v78, v79, 18
	v_ashr_pk_u8_i32 v72, v72, v73, 18
	v_ashr_pk_u8_i32 v74, v74, v75, 18
	v_ashr_pk_u8_i32 v68, v68, v69, 18
	v_ashr_pk_u8_i32 v70, v70, v71, 18
	v_and_b32_e32 v80, 0xffff, v80
	v_lshl_or_b32 v100, v82, 16, v80
	v_and_b32_e32 v76, 0xffff, v76
	v_lshl_or_b32 v101, v78, 16, v76
	v_and_b32_e32 v72, 0xffff, v72
	v_lshl_or_b32 v102, v74, 16, v72
	v_and_b32_e32 v68, 0xffff, v68
	v_lshl_or_b32 v103, v70, 16, v68
	global_store_dwordx4 v[106:107], v[100:103], off

.LBB0_885:
	s_waitcnt lgkmcnt(1)
	s_waitcnt lgkmcnt(0)
	s_mov_b32 s98, 0xbfb8aa3b
	s_mov_b32 s99, 0xbfb8aa3b
	v_pk_fma_f32 v[64:65], v[64:65], s[98:99], v[120:121]
	v_pk_fma_f32 v[66:67], v[66:67], s[98:99], v[122:123]
	v_pk_fma_f32 v[60:61], v[60:61], s[98:99], v[116:117]
	v_pk_fma_f32 v[62:63], v[62:63], s[98:99], v[118:119]
	v_pk_fma_f32 v[56:57], v[56:57], s[98:99], v[124:125]
	v_pk_fma_f32 v[58:59], v[58:59], s[98:99], v[126:127]
	v_pk_fma_f32 v[52:53], v[52:53], s[98:99], v[128:129]
	v_pk_fma_f32 v[54:55], v[54:55], s[98:99], v[130:131]
	v_mov_b32_e32 v124, 1.0
	v_mov_b32_e32 v125, 1.0
	v_mov_b32_e32 v133, v142
	s_add_i32 s19, s87, -11
	s_lshr_b32 s20, s19, 2
	v_mov_b32_e32 v120, s20
	v_mov_b32_e32 v121, v3
	v_mad_i64_i32 v[120:121], s[20:21], v138, 3, v[120:121]
	v_lshlrev_b64 v[120:121], 10, v[120:121]
	s_lshl_b32 s19, s19, 8
	s_and_b32 s34, s19, 0x300
	v_lshl_add_u64 v[120:121], s[46:47], 0, v[120:121]
	v_lshl_add_u64 v[120:121], v[120:121], 0, s[34:35]
	v_lshl_add_u64 v[122:123], v[120:121], 0, v[2:3]
	v_exp_f32_e32 v64, v64
	v_exp_f32_e32 v65, v65
	v_exp_f32_e32 v66, v66
	v_exp_f32_e32 v67, v67
	v_exp_f32_e32 v60, v60
	v_exp_f32_e32 v61, v61
	v_exp_f32_e32 v62, v62
	v_exp_f32_e32 v63, v63
	v_exp_f32_e32 v56, v56
	v_exp_f32_e32 v57, v57
	v_exp_f32_e32 v58, v58
	v_exp_f32_e32 v59, v59
	v_exp_f32_e32 v52, v52
	v_exp_f32_e32 v53, v53
	v_exp_f32_e32 v54, v54
	v_exp_f32_e32 v55, v55
	v_pk_add_f32 v[64:65], v[64:65], v[124:125]
	v_pk_add_f32 v[66:67], v[66:67], v[124:125]
	v_pk_add_f32 v[60:61], v[60:61], v[124:125]
	v_pk_add_f32 v[62:63], v[62:63], v[124:125]
	v_pk_add_f32 v[56:57], v[56:57], v[124:125]
	v_pk_add_f32 v[58:59], v[58:59], v[124:125]
	v_pk_add_f32 v[52:53], v[52:53], v[124:125]
	v_pk_add_f32 v[54:55], v[54:55], v[124:125]
	v_rcp_f32_e32 v64, v64
	v_rcp_f32_e32 v65, v65
	v_rcp_f32_e32 v66, v66
	v_rcp_f32_e32 v67, v67
	v_rcp_f32_e32 v60, v60
	v_rcp_f32_e32 v61, v61
	v_rcp_f32_e32 v62, v62
	v_rcp_f32_e32 v63, v63
	v_rcp_f32_e32 v56, v56
	v_rcp_f32_e32 v57, v57
	v_rcp_f32_e32 v58, v58
	v_rcp_f32_e32 v59, v59
	v_rcp_f32_e32 v52, v52
	v_rcp_f32_e32 v53, v53
	v_rcp_f32_e32 v54, v54
	v_rcp_f32_e32 v55, v55
	v_add_u32_e32 v64, 0xc4820000, v64
	v_add_u32_e32 v65, 0xc4820000, v65
	v_add_u32_e32 v66, 0xc4820000, v66
	v_add_u32_e32 v67, 0xc4820000, v67
	v_add_u32_e32 v60, 0xc4820000, v60
	v_add_u32_e32 v61, 0xc4820000, v61
	v_add_u32_e32 v62, 0xc4820000, v62
	v_add_u32_e32 v63, 0xc4820000, v63
	v_add_u32_e32 v56, 0xc4820000, v56
	v_add_u32_e32 v57, 0xc4820000, v57
	v_add_u32_e32 v58, 0xc4820000, v58
	v_add_u32_e32 v59, 0xc4820000, v59
	v_add_u32_e32 v52, 0xc4820000, v52
	v_add_u32_e32 v53, 0xc4820000, v53
	v_add_u32_e32 v54, 0xc4820000, v54
	v_add_u32_e32 v55, 0xc4820000, v55
	v_ashr_pk_u8_i32 v64, v64, v65, 18
	v_ashr_pk_u8_i32 v66, v66, v67, 18
	v_ashr_pk_u8_i32 v60, v60, v61, 18
	v_ashr_pk_u8_i32 v62, v62, v63, 18
	v_ashr_pk_u8_i32 v56, v56, v57, 18
	v_ashr_pk_u8_i32 v58, v58, v59, 18
	v_ashr_pk_u8_i32 v52, v52, v53, 18
	v_ashr_pk_u8_i32 v54, v54, v55, 18
	v_and_b32_e32 v64, 0xffff, v64
	v_lshl_or_b32 v116, v66, 16, v64
	v_and_b32_e32 v60, 0xffff, v60
	v_lshl_or_b32 v117, v62, 16, v60
	v_and_b32_e32 v56, 0xffff, v56
	v_lshl_or_b32 v118, v58, 16, v56
	v_and_b32_e32 v52, 0xffff, v52
	v_lshl_or_b32 v119, v54, 16, v52
	global_store_dwordx4 v[122:123], v[116:119], off
	s_and_b64 vcc, exec, s[40:41]
	s_mov_b64 s[26:27], -1
	s_cbranch_vccz .LBB0_950

.LBB0_887:
	s_waitcnt lgkmcnt(1)
	s_waitcnt lgkmcnt(0)
	s_mov_b32 s98, 0xbfb8aa3b
	s_mov_b32 s99, 0xbfb8aa3b
	v_pk_fma_f32 v[48:49], v[48:49], s[98:99], v[104:105]
	v_pk_fma_f32 v[50:51], v[50:51], s[98:99], v[106:107]
	v_pk_fma_f32 v[44:45], v[44:45], s[98:99], v[100:101]
	v_pk_fma_f32 v[46:47], v[46:47], s[98:99], v[102:103]
	v_pk_fma_f32 v[40:41], v[40:41], s[98:99], v[108:109]
	v_pk_fma_f32 v[42:43], v[42:43], s[98:99], v[110:111]
	v_pk_fma_f32 v[36:37], v[36:37], s[98:99], v[112:113]
	v_pk_fma_f32 v[38:39], v[38:39], s[98:99], v[114:115]
	v_mov_b32_e32 v108, 1.0
	v_mov_b32_e32 v109, 1.0
	v_mov_b32_e32 v54, v133
	s_add_i32 s19, s87, -11
	s_lshr_b32 s20, s19, 2
	v_mov_b32_e32 v104, s20
	v_mov_b32_e32 v105, v3
	v_mad_i64_i32 v[104:105], s[20:21], v136, 3, v[104:105]
	v_lshlrev_b64 v[104:105], 10, v[104:105]
	s_lshl_b32 s19, s19, 8
	s_and_b32 s34, s19, 0x300
	v_lshl_add_u64 v[104:105], s[46:47], 0, v[104:105]
	v_lshl_add_u64 v[104:105], v[104:105], 0, s[34:35]
	v_lshl_add_u64 v[106:107], v[104:105], 0, v[2:3]
	v_exp_f32_e32 v48, v48
	v_exp_f32_e32 v49, v49
	v_exp_f32_e32 v50, v50
	v_exp_f32_e32 v51, v51
	v_exp_f32_e32 v44, v44
	v_exp_f32_e32 v45, v45
	v_exp_f32_e32 v46, v46
	v_exp_f32_e32 v47, v47
	v_exp_f32_e32 v40, v40
	v_exp_f32_e32 v41, v41
	v_exp_f32_e32 v42, v42
	v_exp_f32_e32 v43, v43
	v_exp_f32_e32 v36, v36
	v_exp_f32_e32 v37, v37
	v_exp_f32_e32 v38, v38
	v_exp_f32_e32 v39, v39
	v_pk_add_f32 v[48:49], v[48:49], v[108:109]
	v_pk_add_f32 v[50:51], v[50:51], v[108:109]
	v_pk_add_f32 v[44:45], v[44:45], v[108:109]
	v_pk_add_f32 v[46:47], v[46:47], v[108:109]
	v_pk_add_f32 v[40:41], v[40:41], v[108:109]
	v_pk_add_f32 v[42:43], v[42:43], v[108:109]
	v_pk_add_f32 v[36:37], v[36:37], v[108:109]
	v_pk_add_f32 v[38:39], v[38:39], v[108:109]
	v_rcp_f32_e32 v48, v48
	v_rcp_f32_e32 v49, v49
	v_rcp_f32_e32 v50, v50
	v_rcp_f32_e32 v51, v51
	v_rcp_f32_e32 v44, v44
	v_rcp_f32_e32 v45, v45
	v_rcp_f32_e32 v46, v46
	v_rcp_f32_e32 v47, v47
	v_rcp_f32_e32 v40, v40
	v_rcp_f32_e32 v41, v41
	v_rcp_f32_e32 v42, v42
	v_rcp_f32_e32 v43, v43
	v_rcp_f32_e32 v36, v36
	v_rcp_f32_e32 v37, v37
	v_rcp_f32_e32 v38, v38
	v_rcp_f32_e32 v39, v39
	v_add_u32_e32 v48, 0xc4820000, v48
	v_add_u32_e32 v49, 0xc4820000, v49
	v_add_u32_e32 v50, 0xc4820000, v50
	v_add_u32_e32 v51, 0xc4820000, v51
	v_add_u32_e32 v44, 0xc4820000, v44
	v_add_u32_e32 v45, 0xc4820000, v45
	v_add_u32_e32 v46, 0xc4820000, v46
	v_add_u32_e32 v47, 0xc4820000, v47
	v_add_u32_e32 v40, 0xc4820000, v40
	v_add_u32_e32 v41, 0xc4820000, v41
	v_add_u32_e32 v42, 0xc4820000, v42
	v_add_u32_e32 v43, 0xc4820000, v43
	v_add_u32_e32 v36, 0xc4820000, v36
	v_add_u32_e32 v37, 0xc4820000, v37
	v_add_u32_e32 v38, 0xc4820000, v38
	v_add_u32_e32 v39, 0xc4820000, v39
	v_ashr_pk_u8_i32 v48, v48, v49, 18
	v_ashr_pk_u8_i32 v50, v50, v51, 18
	v_ashr_pk_u8_i32 v44, v44, v45, 18
	v_ashr_pk_u8_i32 v46, v46, v47, 18
	v_ashr_pk_u8_i32 v40, v40, v41, 18
	v_ashr_pk_u8_i32 v42, v42, v43, 18
	v_ashr_pk_u8_i32 v36, v36, v37, 18
	v_ashr_pk_u8_i32 v38, v38, v39, 18
	v_and_b32_e32 v48, 0xffff, v48
	v_lshl_or_b32 v100, v50, 16, v48
	v_and_b32_e32 v44, 0xffff, v44
	v_lshl_or_b32 v101, v46, 16, v44
	v_and_b32_e32 v40, 0xffff, v40
	v_lshl_or_b32 v102, v42, 16, v40
	v_and_b32_e32 v36, 0xffff, v36
	v_lshl_or_b32 v103, v38, 16, v36
	global_store_dwordx4 v[106:107], v[100:103], off
	s_and_b64 vcc, exec, s[40:41]
	s_mov_b64 s[26:27], -1
	s_cbranch_vccz .LBB0_1000

.LBB0_889:
	s_waitcnt lgkmcnt(1)
	s_waitcnt lgkmcnt(0)
	s_mov_b32 s98, 0xbfb8aa3b
	s_mov_b32 s99, 0xbfb8aa3b
	v_pk_fma_f32 v[32:33], v[32:33], s[98:99], v[88:89]
	v_pk_fma_f32 v[34:35], v[34:35], s[98:99], v[90:91]
	v_pk_fma_f32 v[28:29], v[28:29], s[98:99], v[84:85]
	v_pk_fma_f32 v[30:31], v[30:31], s[98:99], v[86:87]
	v_pk_fma_f32 v[24:25], v[24:25], s[98:99], v[92:93]
	v_pk_fma_f32 v[26:27], v[26:27], s[98:99], v[94:95]
	v_pk_fma_f32 v[20:21], v[20:21], s[98:99], v[96:97]
	v_pk_fma_f32 v[22:23], v[22:23], s[98:99], v[98:99]
	v_mov_b32_e32 v92, 1.0
	v_mov_b32_e32 v93, 1.0
	v_mov_b32_e32 v38, v54
	s_add_i32 s19, s87, -11
	s_lshr_b32 s20, s19, 2
	v_mov_b32_e32 v88, s20
	v_mov_b32_e32 v89, v3
	v_mad_i64_i32 v[88:89], s[20:21], v134, 3, v[88:89]
	v_lshlrev_b64 v[88:89], 10, v[88:89]
	s_lshl_b32 s19, s19, 8
	s_and_b32 s34, s19, 0x300
	v_lshl_add_u64 v[88:89], s[46:47], 0, v[88:89]
	v_lshl_add_u64 v[88:89], v[88:89], 0, s[34:35]
	v_lshl_add_u64 v[90:91], v[88:89], 0, v[2:3]
	v_exp_f32_e32 v32, v32
	v_exp_f32_e32 v33, v33
	v_exp_f32_e32 v34, v34
	v_exp_f32_e32 v35, v35
	v_exp_f32_e32 v28, v28
	v_exp_f32_e32 v29, v29
	v_exp_f32_e32 v30, v30
	v_exp_f32_e32 v31, v31
	v_exp_f32_e32 v24, v24
	v_exp_f32_e32 v25, v25
	v_exp_f32_e32 v26, v26
	v_exp_f32_e32 v27, v27
	v_exp_f32_e32 v20, v20
	v_exp_f32_e32 v21, v21
	v_exp_f32_e32 v22, v22
	v_exp_f32_e32 v23, v23
	v_pk_add_f32 v[32:33], v[32:33], v[92:93]
	v_pk_add_f32 v[34:35], v[34:35], v[92:93]
	v_pk_add_f32 v[28:29], v[28:29], v[92:93]
	v_pk_add_f32 v[30:31], v[30:31], v[92:93]
	v_pk_add_f32 v[24:25], v[24:25], v[92:93]
	v_pk_add_f32 v[26:27], v[26:27], v[92:93]
	v_pk_add_f32 v[20:21], v[20:21], v[92:93]
	v_pk_add_f32 v[22:23], v[22:23], v[92:93]
	v_rcp_f32_e32 v32, v32
	v_rcp_f32_e32 v33, v33
	v_rcp_f32_e32 v34, v34
	v_rcp_f32_e32 v35, v35
	v_rcp_f32_e32 v28, v28
	v_rcp_f32_e32 v29, v29
	v_rcp_f32_e32 v30, v30
	v_rcp_f32_e32 v31, v31
	v_rcp_f32_e32 v24, v24
	v_rcp_f32_e32 v25, v25
	v_rcp_f32_e32 v26, v26
	v_rcp_f32_e32 v27, v27
	v_rcp_f32_e32 v20, v20
	v_rcp_f32_e32 v21, v21
	v_rcp_f32_e32 v22, v22
	v_rcp_f32_e32 v23, v23
	v_add_u32_e32 v32, 0xc4820000, v32
	v_add_u32_e32 v33, 0xc4820000, v33
	v_add_u32_e32 v34, 0xc4820000, v34
	v_add_u32_e32 v35, 0xc4820000, v35
	v_add_u32_e32 v28, 0xc4820000, v28
	v_add_u32_e32 v29, 0xc4820000, v29
	v_add_u32_e32 v30, 0xc4820000, v30
	v_add_u32_e32 v31, 0xc4820000, v31
	v_add_u32_e32 v24, 0xc4820000, v24
	v_add_u32_e32 v25, 0xc4820000, v25
	v_add_u32_e32 v26, 0xc4820000, v26
	v_add_u32_e32 v27, 0xc4820000, v27
	v_add_u32_e32 v20, 0xc4820000, v20
	v_add_u32_e32 v21, 0xc4820000, v21
	v_add_u32_e32 v22, 0xc4820000, v22
	v_add_u32_e32 v23, 0xc4820000, v23
	v_ashr_pk_u8_i32 v32, v32, v33, 18
	v_ashr_pk_u8_i32 v34, v34, v35, 18
	v_ashr_pk_u8_i32 v28, v28, v29, 18
	v_ashr_pk_u8_i32 v30, v30, v31, 18
	v_ashr_pk_u8_i32 v24, v24, v25, 18
	v_ashr_pk_u8_i32 v26, v26, v27, 18
	v_ashr_pk_u8_i32 v20, v20, v21, 18
	v_ashr_pk_u8_i32 v22, v22, v23, 18
	v_and_b32_e32 v32, 0xffff, v32
	v_lshl_or_b32 v84, v34, 16, v32
	v_and_b32_e32 v28, 0xffff, v28
	v_lshl_or_b32 v85, v30, 16, v28
	v_and_b32_e32 v24, 0xffff, v24
	v_lshl_or_b32 v86, v26, 16, v24
	v_and_b32_e32 v20, 0xffff, v20
	v_lshl_or_b32 v87, v22, 16, v20
	global_store_dwordx4 v[90:91], v[84:87], off
	s_and_b64 vcc, exec, s[40:41]
	s_mov_b64 s[26:27], -1
	s_cbranch_vccz .LBB0_1050

.LBB0_891:
	s_waitcnt lgkmcnt(1)
	s_waitcnt lgkmcnt(0)
	s_mov_b32 s98, 0xbfb8aa3b
	s_mov_b32 s99, 0xbfb8aa3b
	v_pk_fma_f32 v[16:17], v[16:17], s[98:99], v[72:73]
	v_pk_fma_f32 v[18:19], v[18:19], s[98:99], v[74:75]
	v_pk_fma_f32 v[12:13], v[12:13], s[98:99], v[68:69]
	v_pk_fma_f32 v[14:15], v[14:15], s[98:99], v[70:71]
	v_pk_fma_f32 v[8:9], v[8:9], s[98:99], v[76:77]
	v_pk_fma_f32 v[10:11], v[10:11], s[98:99], v[78:79]
	v_pk_fma_f32 v[4:5], v[4:5], s[98:99], v[80:81]
	v_pk_fma_f32 v[6:7], v[6:7], s[98:99], v[82:83]
	v_mov_b32_e32 v76, 1.0
	v_mov_b32_e32 v77, 1.0
	v_mov_b32_e32 v28, v38
	s_add_i32 s87, s87, -11
	s_lshr_b32 s19, s87, 2
	v_mov_b32_e32 v72, s19
	v_mov_b32_e32 v73, v3
	v_mad_i64_i32 v[72:73], s[20:21], v132, 3, v[72:73]
	v_lshlrev_b64 v[72:73], 10, v[72:73]
	s_lshl_b32 s19, s87, 8
	s_and_b32 s34, s19, 0x300
	v_lshl_add_u64 v[72:73], s[46:47], 0, v[72:73]
	v_lshl_add_u64 v[72:73], v[72:73], 0, s[34:35]
	v_lshl_add_u64 v[74:75], v[72:73], 0, v[2:3]
	v_exp_f32_e32 v16, v16
	v_exp_f32_e32 v17, v17
	v_exp_f32_e32 v18, v18
	v_exp_f32_e32 v19, v19
	v_exp_f32_e32 v12, v12
	v_exp_f32_e32 v13, v13
	v_exp_f32_e32 v14, v14
	v_exp_f32_e32 v15, v15
	v_exp_f32_e32 v8, v8
	v_exp_f32_e32 v9, v9
	v_exp_f32_e32 v10, v10
	v_exp_f32_e32 v11, v11
	v_exp_f32_e32 v4, v4
	v_exp_f32_e32 v5, v5
	v_exp_f32_e32 v6, v6
	v_exp_f32_e32 v7, v7
	v_pk_add_f32 v[16:17], v[16:17], v[76:77]
	v_pk_add_f32 v[18:19], v[18:19], v[76:77]
	v_pk_add_f32 v[12:13], v[12:13], v[76:77]
	v_pk_add_f32 v[14:15], v[14:15], v[76:77]
	v_pk_add_f32 v[8:9], v[8:9], v[76:77]
	v_pk_add_f32 v[10:11], v[10:11], v[76:77]
	v_pk_add_f32 v[4:5], v[4:5], v[76:77]
	v_pk_add_f32 v[6:7], v[6:7], v[76:77]
	v_rcp_f32_e32 v16, v16
	v_rcp_f32_e32 v17, v17
	v_rcp_f32_e32 v18, v18
	v_rcp_f32_e32 v19, v19
	v_rcp_f32_e32 v12, v12
	v_rcp_f32_e32 v13, v13
	v_rcp_f32_e32 v14, v14
	v_rcp_f32_e32 v15, v15
	v_rcp_f32_e32 v8, v8
	v_rcp_f32_e32 v9, v9
	v_rcp_f32_e32 v10, v10
	v_rcp_f32_e32 v11, v11
	v_rcp_f32_e32 v4, v4
	v_rcp_f32_e32 v5, v5
	v_rcp_f32_e32 v6, v6
	v_rcp_f32_e32 v7, v7
	v_add_u32_e32 v16, 0xc4820000, v16
	v_add_u32_e32 v17, 0xc4820000, v17
	v_add_u32_e32 v18, 0xc4820000, v18
	v_add_u32_e32 v19, 0xc4820000, v19
	v_add_u32_e32 v12, 0xc4820000, v12
	v_add_u32_e32 v13, 0xc4820000, v13
	v_add_u32_e32 v14, 0xc4820000, v14
	v_add_u32_e32 v15, 0xc4820000, v15
	v_add_u32_e32 v8, 0xc4820000, v8
	v_add_u32_e32 v9, 0xc4820000, v9
	v_add_u32_e32 v10, 0xc4820000, v10
	v_add_u32_e32 v11, 0xc4820000, v11
	v_add_u32_e32 v4, 0xc4820000, v4
	v_add_u32_e32 v5, 0xc4820000, v5
	v_add_u32_e32 v6, 0xc4820000, v6
	v_add_u32_e32 v7, 0xc4820000, v7
	v_ashr_pk_u8_i32 v16, v16, v17, 18
	v_ashr_pk_u8_i32 v18, v18, v19, 18
	v_ashr_pk_u8_i32 v12, v12, v13, 18
	v_ashr_pk_u8_i32 v14, v14, v15, 18
	v_ashr_pk_u8_i32 v8, v8, v9, 18
	v_ashr_pk_u8_i32 v10, v10, v11, 18
	v_ashr_pk_u8_i32 v4, v4, v5, 18
	v_ashr_pk_u8_i32 v6, v6, v7, 18
	v_and_b32_e32 v16, 0xffff, v16
	v_lshl_or_b32 v68, v18, 16, v16
	v_and_b32_e32 v12, 0xffff, v12
	v_lshl_or_b32 v69, v14, 16, v12
	v_and_b32_e32 v8, 0xffff, v8
	v_lshl_or_b32 v70, v10, 16, v8
	v_and_b32_e32 v4, 0xffff, v4
	v_lshl_or_b32 v71, v6, 16, v4
	global_store_dwordx4 v[74:75], v[68:71], off

.LBB0_2141:
	v_mov_b32_e32 v131, 0
	s_andn2_b64 vcc, exec, s[46:47]
	v_mov_b32_e32 v130, v131
	v_mov_b32_e32 v129, v131
	v_mov_b32_e32 v128, v131
	v_mov_b32_e32 v127, v131
	v_mov_b32_e32 v126, v131
	v_mov_b32_e32 v125, v131
	v_mov_b32_e32 v124, v131
	v_mov_b32_e32 v115, v131
	v_mov_b32_e32 v114, v131
	v_mov_b32_e32 v113, v131
	v_mov_b32_e32 v112, v131
	v_mov_b32_e32 v111, v131
	v_mov_b32_e32 v110, v131
	v_mov_b32_e32 v109, v131
	v_mov_b32_e32 v108, v131
	v_mov_b32_e32 v99, v131
	v_mov_b32_e32 v98, v131
	v_mov_b32_e32 v97, v131
	v_mov_b32_e32 v96, v131
	v_mov_b32_e32 v95, v131
	v_mov_b32_e32 v94, v131
	v_mov_b32_e32 v93, v131
	v_mov_b32_e32 v92, v131
	v_mov_b32_e32 v83, v131
	v_mov_b32_e32 v82, v131
	v_mov_b32_e32 v81, v131
	v_mov_b32_e32 v80, v131
	v_mov_b32_e32 v79, v131
	v_mov_b32_e32 v78, v131
	v_mov_b32_e32 v77, v131
	v_mov_b32_e32 v76, v131
	v_mov_b32_e32 v123, v131
	v_mov_b32_e32 v122, v131
	v_mov_b32_e32 v121, v131
	v_mov_b32_e32 v120, v131
	v_mov_b32_e32 v119, v131
	v_mov_b32_e32 v118, v131
	v_mov_b32_e32 v117, v131
	v_mov_b32_e32 v116, v131
	v_mov_b32_e32 v107, v131
	v_mov_b32_e32 v106, v131
	v_mov_b32_e32 v105, v131
	v_mov_b32_e32 v104, v131
	v_mov_b32_e32 v103, v131
	v_mov_b32_e32 v102, v131
	v_mov_b32_e32 v101, v131
	v_mov_b32_e32 v100, v131
	v_mov_b32_e32 v91, v131
	v_mov_b32_e32 v90, v131
	v_mov_b32_e32 v89, v131
	v_mov_b32_e32 v88, v131
	v_mov_b32_e32 v87, v131
	v_mov_b32_e32 v86, v131
	v_mov_b32_e32 v85, v131
	v_mov_b32_e32 v84, v131
	v_mov_b32_e32 v75, v131
	v_mov_b32_e32 v74, v131
	v_mov_b32_e32 v73, v131
	v_mov_b32_e32 v72, v131
	v_mov_b32_e32 v71, v131
	v_mov_b32_e32 v70, v131
	v_mov_b32_e32 v69, v131
	v_mov_b32_e32 v68, v131
	v_mov_b32_e32 v67, v131
	v_mov_b32_e32 v66, v131
	v_mov_b32_e32 v65, v131
	v_mov_b32_e32 v64, v131
	v_mov_b32_e32 v63, v131
	v_mov_b32_e32 v62, v131
	v_mov_b32_e32 v61, v131
	v_mov_b32_e32 v60, v131
	v_mov_b32_e32 v51, v131
	v_mov_b32_e32 v50, v131
	v_mov_b32_e32 v49, v131
	v_mov_b32_e32 v48, v131
	v_mov_b32_e32 v47, v131
	v_mov_b32_e32 v46, v131
	v_mov_b32_e32 v45, v131
	v_mov_b32_e32 v44, v131
	v_mov_b32_e32 v35, v131
	v_mov_b32_e32 v34, v131
	v_mov_b32_e32 v33, v131
	v_mov_b32_e32 v32, v131
	v_mov_b32_e32 v31, v131
	v_mov_b32_e32 v30, v131
	v_mov_b32_e32 v29, v131
	v_mov_b32_e32 v28, v131
	v_mov_b32_e32 v19, v131
	v_mov_b32_e32 v18, v131
	v_mov_b32_e32 v17, v131
	v_mov_b32_e32 v16, v131
	v_mov_b32_e32 v15, v131
	v_mov_b32_e32 v14, v131
	v_mov_b32_e32 v13, v131
	v_mov_b32_e32 v12, v131
	v_mov_b32_e32 v59, v131
	v_mov_b32_e32 v58, v131
	v_mov_b32_e32 v57, v131
	v_mov_b32_e32 v56, v131
	v_mov_b32_e32 v55, v131
	v_mov_b32_e32 v54, v131
	v_mov_b32_e32 v53, v131
	v_mov_b32_e32 v52, v131
	v_mov_b32_e32 v43, v131
	v_mov_b32_e32 v42, v131
	v_mov_b32_e32 v41, v131
	v_mov_b32_e32 v40, v131
	v_mov_b32_e32 v39, v131
	v_mov_b32_e32 v38, v131
	v_mov_b32_e32 v37, v131
	v_mov_b32_e32 v36, v131
	v_mov_b32_e32 v27, v131
	v_mov_b32_e32 v26, v131
	v_mov_b32_e32 v25, v131
	v_mov_b32_e32 v24, v131
	v_mov_b32_e32 v23, v131
	v_mov_b32_e32 v22, v131
	v_mov_b32_e32 v21, v131
	v_mov_b32_e32 v20, v131
	v_mov_b32_e32 v11, v131
	v_mov_b32_e32 v10, v131
	v_mov_b32_e32 v9, v131
	v_mov_b32_e32 v8, v131
	v_mov_b32_e32 v7, v131
	v_mov_b32_e32 v6, v131
	v_mov_b32_e32 v5, v131
	v_mov_b32_e32 v4, v131
	s_cbranch_vccnz .LBB0_2144
	s_add_u32 s26, s26, 0x80
	s_addc_u32 s27, s27, 0
	s_add_u32 s19, s30, 0x100
	s_addc_u32 s20, s31, 0
	s_mov_b32 s21, 0
